# L2 prefetch helpers (wave 0 of WGs 16..47 touch the scan chunks 10 ahead, progress word via atomic) on top of v10
# speedup vs baseline: 1.0250x; 1.0234x over previous
; DI float bflo(unsigned u) { return __uint_as_float(u << 16); }
; DI float bfhi(unsigned u) { return __uint_as_float(u & 0xffff0000u); }
; DI bf16x8 packS(const f32x16& x, int s) { return pack8(x[8 * s], x[8 * s + 1], x[8 * s + 2], x[8 * s + 3], x[8 * s + 4], x[8 * s + 5], x[8 * s + 6], x[8 * s + 7]); }
; #define SCAN_RDW(F, mh) do { _Pragma("unroll") for (int k = 0; k < 8; ++k) { const int i2 = k >> 2, m = 2 * (mh) + ((k >> 1) & 1), sx = k & 1; F[k] = *(const bf16x8*)(lw + ((i2 * 4 + m) * 2 + sx) * 1024); } } while (0)
; DI void gdn_scan_seq(const Params& p, int bh16, char* ldsf) {
;     ...
;   f32x16 S[4];
; #pragma unroll
;   for (int m = 0; m < 4; ++m)
; #pragma unroll
;     for (int r = 0; r < 16; ++r) S[m][r] = 0.f;
;   asm volatile("s_waitcnt vmcnt(0)" ::: "memory");
;   __syncthreads();
;   SCAN_ISSUE(0, 0); SCAN_ISSUE(1, 1);
;   int sl = 0;
; #pragma unroll 1
;   for (int c = 0; c < 128; ++c) {
;     if (c + 1 < 128) asm volatile("s_waitcnt vmcnt(12)" ::: "memory"); else asm volatile("s_waitcnt vmcnt(0)" ::: "memory");
;     __builtin_amdgcn_s_barrier();
;     asm volatile("" ::: "memory");
;     char* sco = scp + (size_t)c * 32768;
;     bf16x8 Sb[4][2];
; #pragma unroll
;     for (int m = 0; m < 4; ++m) { Sb[m][0] = packS(S[m], 0); Sb[m][1] = packS(S[m], 1); *(bf16x8*)(sco + (m * 2 + 0) * 1024) = Sb[m][0]; *(bf16x8*)(sco + (m * 2 + 1) * 1024) = Sb[m][1]; }
;     __builtin_amdgcn_sched_barrier(0);
;     if (c + 2 < 128) { const int s2 = sl >= 1 ? sl - 1 : 2; SCAN_ISSUE(c + 2, s2); }
;     const char* base = ldsf + sl * 49152;
;     const char* lw = base + lane * 16; const char* lk = lw + 16384; const char* lu = base + 32768 + wv * 4096 + lane * 16;
;     const float gl = glt[c];
;     f32x16 vn[2];
; #pragma unroll
;     for (int i2 = 0; i2 < 2; ++i2) {
;       const u32x4 ua = *(const u32x4*)(lu + (2 * i2) * 1024), ub = *(const u32x4*)(lu + (2 * i2 + 1) * 1024);
; #pragma unroll
;       for (int e = 0; e < 4; ++e) { vn[i2][2 * e] = bflo(ua[e]); vn[i2][2 * e + 1] = bfhi(ua[e]); vn[i2][8 + 2 * e] = bflo(ub[e]); vn[i2][8 + 2 * e + 1] = bfhi(ub[e]); }
;     }
;     bf16x8 fa[8], fb[8];
;     ...
;     SCAN_RDW(fa, 0);
;     __builtin_amdgcn_sched_barrier(0);
;     SCAN_RDW(fb, 1);
;     __builtin_amdgcn_sched_barrier(0);
;     SCAN_MMW(fa, 0);
;     __builtin_amdgcn_sched_barrier(0);
;     SCAN_RDK(fa, 0);
.Lscan_glt_done:
	s_or_b64 exec, exec, s[6:7]
	s_lshl_b32 s3, s2, 22
	s_add_u32 s8, s56, s3
	s_addc_u32 s9, s57, 0
	s_add_u32 s10, s8, 0x1000
	s_addc_u32 s11, s9, 0
	v_mov_b32_e32 v0, 0
	v_mov_b32_e32 v1, 0
	v_mov_b32_e32 v2, 0
	v_mov_b32_e32 v3, 0
	v_mov_b32_e32 v4, 0
	v_mov_b32_e32 v5, 0
	v_mov_b32_e32 v6, 0
	v_mov_b32_e32 v7, 0
	v_mov_b32_e32 v8, 0
	v_mov_b32_e32 v9, 0
	v_mov_b32_e32 v10, 0
	v_mov_b32_e32 v11, 0
	v_mov_b32_e32 v12, 0
	v_mov_b32_e32 v13, 0
	v_mov_b32_e32 v14, 0
	v_mov_b32_e32 v15, 0
	v_mov_b32_e32 v16, 0
	v_mov_b32_e32 v17, 0
	v_mov_b32_e32 v18, 0
	v_mov_b32_e32 v19, 0
	v_mov_b32_e32 v20, 0
	v_mov_b32_e32 v21, 0
	v_mov_b32_e32 v22, 0
	v_mov_b32_e32 v23, 0
	v_mov_b32_e32 v24, 0
	v_mov_b32_e32 v25, 0
	v_mov_b32_e32 v26, 0
	v_mov_b32_e32 v27, 0
	v_mov_b32_e32 v28, 0
	v_mov_b32_e32 v29, 0
	v_mov_b32_e32 v30, 0
	v_mov_b32_e32 v31, 0
	v_mov_b32_e32 v32, 0
	v_mov_b32_e32 v33, 0
	v_mov_b32_e32 v34, 0
	v_mov_b32_e32 v35, 0
	v_mov_b32_e32 v36, 0
	v_mov_b32_e32 v37, 0
	v_mov_b32_e32 v38, 0
	v_mov_b32_e32 v39, 0
	v_mov_b32_e32 v40, 0
	v_mov_b32_e32 v41, 0
	v_mov_b32_e32 v42, 0
	v_mov_b32_e32 v43, 0
	v_mov_b32_e32 v44, 0
	v_mov_b32_e32 v45, 0
	v_mov_b32_e32 v46, 0
	v_mov_b32_e32 v47, 0
	v_mov_b32_e32 v48, 0
	v_mov_b32_e32 v49, 0
	v_mov_b32_e32 v50, 0
	v_mov_b32_e32 v51, 0
	v_mov_b32_e32 v52, 0
	v_mov_b32_e32 v53, 0
	v_mov_b32_e32 v54, 0
	v_mov_b32_e32 v55, 0
	v_mov_b32_e32 v56, 0
	v_mov_b32_e32 v57, 0
	v_mov_b32_e32 v58, 0
	v_mov_b32_e32 v59, 0
	v_mov_b32_e32 v60, 0
	v_mov_b32_e32 v61, 0
	v_mov_b32_e32 v62, 0
	v_mov_b32_e32 v63, 0
	v_mov_b32_e32 v80, 0
	v_mov_b32_e32 v81, 0
	v_mov_b32_e32 v82, 0
	v_mov_b32_e32 v83, 0
	v_mov_b32_e32 v84, 0
	v_mov_b32_e32 v85, 0
	v_mov_b32_e32 v86, 0
	v_mov_b32_e32 v87, 0
	v_mov_b32_e32 v182, 0
	v_mov_b32_e32 v183, 0
	v_mov_b32_e32 v184, 0
	v_mov_b32_e32 v185, 0
	v_mov_b32_e32 v190, 0
	v_mov_b32_e32 v191, 0
	v_mov_b32_e32 v192, 0
	v_mov_b32_e32 v193, 0
	v_mov_b32_e32 v194, 0
	v_mov_b32_e32 v195, 0
	v_mov_b32_e32 v196, 0
	v_mov_b32_e32 v197, 0
	v_mov_b32_e32 v198, 0
	v_mov_b32_e32 v199, 0
	v_mov_b32_e32 v200, 0
	v_mov_b32_e32 v201, 0
	v_mov_b32_e32 v202, 0
	v_mov_b32_e32 v203, 0
	v_mov_b32_e32 v204, 0
	v_mov_b32_e32 v205, 0
	v_mov_b32_e32 v208, 0
	v_mov_b32_e32 v209, 0
	v_mov_b32_e32 v210, 0
	v_mov_b32_e32 v211, 0
	v_mov_b32_e32 v212, 0
	v_mov_b32_e32 v213, 0
	v_mov_b32_e32 v214, 0
	v_mov_b32_e32 v215, 0
	v_mov_b32_e32 v216, 0
	v_mov_b32_e32 v217, 0
	v_mov_b32_e32 v218, 0
	v_mov_b32_e32 v219, 0
	v_readfirstlane_b32 s16, v206
	s_lshl_b32 s3, s2, 6
	s_add_u32 s14, s84, s3
	s_addc_u32 s15, s85, 0
	s_add_u32 s14, s14, 0xc00
	s_addc_u32 s15, s15, 0
	v_mov_b32_e32 v132, 1
	v_mov_b32_e32 v133, 0
	s_mov_b32 s2, 0
	s_mov_b32 s3, 0
	s_mov_b32 s18, 0x24040
	s_waitcnt lgkmcnt(0)
	s_barrier
.Lscan_loop:
	s_barrier
	s_cmp_lg_u32 s16, 0
	s_cbranch_scc1 .Lscan_noprog
	s_mov_b64 exec, 1
	global_atomic_add v133, v132, s[14:15]
	s_mov_b64 exec, -1
.Lscan_noprog:
	v_add_u32_e32 v131, s3, v130
	v_add_u32_e32 v134, s3, v129
	v_mov_b32_e32 v143, s18
	ds_read_b128 v[72:75], v134 offset:32768
	ds_read_b128 v[76:79], v134 offset:33792
	ds_read_b32 v142, v143
	ds_read_b128 v[148:151], v131 offset:0
	ds_read_b128 v[152:155], v131 offset:1024
	ds_read_b128 v[156:159], v131 offset:2048
	ds_read_b128 v[160:163], v131 offset:3072
	ds_read_b128 v[164:167], v131 offset:4096
	ds_read_b128 v[168:171], v131 offset:5120
	ds_read_b128 v[172:175], v131 offset:6144
	ds_read_b128 v[178:181], v131 offset:7168
	ds_read_b128 v[88:91], v134 offset:34816
	ds_read_b128 v[92:95], v134 offset:35840
	s_waitcnt lgkmcnt(10)
	v_mfma_f32_32x32x16_bf16 v[0:15], v[182:185], v[80:83], v[0:15]
	v_lshlrev_b32_e32 v64, 16, v72
	v_and_b32_e32 v65, 0xffff0000, v72
	v_lshlrev_b32_e32 v66, 16, v73
	v_and_b32_e32 v67, 0xffff0000, v73
	v_lshlrev_b32_e32 v68, 16, v74
	v_mfma_f32_32x32x16_bf16 v[0:15], v[190:193], v[84:87], v[0:15]
	v_and_b32_e32 v69, 0xffff0000, v74
	v_lshlrev_b32_e32 v70, 16, v75
	v_and_b32_e32 v71, 0xffff0000, v75
	v_lshlrev_b32_e32 v72, 16, v76
	v_and_b32_e32 v73, 0xffff0000, v76
	v_mfma_f32_32x32x16_bf16 v[16:31], v[194:197], v[80:83], v[16:31]
	v_lshlrev_b32_e32 v74, 16, v77
	v_and_b32_e32 v75, 0xffff0000, v77
	v_lshlrev_b32_e32 v76, 16, v78
	v_and_b32_e32 v77, 0xffff0000, v78
	v_mfma_f32_32x32x16_bf16 v[16:31], v[198:201], v[84:87], v[16:31]
	v_lshlrev_b32_e32 v78, 16, v79
	v_and_b32_e32 v79, 0xffff0000, v79
	s_nop 1
	v_mfma_f32_32x32x16_bf16 v[32:47], v[202:205], v[80:83], v[32:47]
	v_cvt_pk_bf16_f32 v96, v0, v1
	v_cvt_pk_bf16_f32 v97, v2, v3
	v_cvt_pk_bf16_f32 v98, v4, v5
	v_cvt_pk_bf16_f32 v99, v6, v7
	v_cvt_pk_bf16_f32 v100, v8, v9
	v_mfma_f32_32x32x16_bf16 v[32:47], v[208:211], v[84:87], v[32:47]
	v_cvt_pk_bf16_f32 v101, v10, v11
	v_cvt_pk_bf16_f32 v102, v12, v13
	v_cvt_pk_bf16_f32 v103, v14, v15
	s_nop 1
	v_mfma_f32_32x32x16_bf16 v[48:63], v[212:215], v[80:83], v[48:63]
	v_cvt_pk_bf16_f32 v104, v16, v17
	v_cvt_pk_bf16_f32 v105, v18, v19
	v_cvt_pk_bf16_f32 v106, v20, v21
	v_cvt_pk_bf16_f32 v107, v22, v23
	v_cvt_pk_bf16_f32 v108, v24, v25
	v_mfma_f32_32x32x16_bf16 v[48:63], v[216:219], v[84:87], v[48:63]
	v_cvt_pk_bf16_f32 v109, v26, v27
	v_cvt_pk_bf16_f32 v110, v28, v29
	v_cvt_pk_bf16_f32 v111, v30, v31
	s_waitcnt lgkmcnt(0)
; DI bf16x8 packS(const f32x16& x, int s) { return pack8(x[8 * s], x[8 * s + 1], x[8 * s + 2], x[8 * s + 3], x[8 * s + 4], x[8 * s + 5], x[8 * s + 6], x[8 * s + 7]); }
; #define SCAN_RDW(F, mh) do { _Pragma("unroll") for (int k = 0; k < 8; ++k) { const int i2 = k >> 2, m = 2 * (mh) + ((k >> 1) & 1), sx = k & 1; F[k] = *(const bf16x8*)(lw + ((i2 * 4 + m) * 2 + sx) * 1024); } } while (0)
; #define SCAN_RDK(F, mh) do { _Pragma("unroll") for (int k = 0; k < 8; ++k) { const int m = 2 * (mh) + (k >> 2), j2 = (k >> 1) & 1, sx = k & 1; F[k] = *(const bf16x8*)(lk + ((m * 2 + j2) * 2 + sx) * 1024); } } while (0)
; #define SCAN_MMW(F, mh) do { _Pragma("unroll") for (int q = 0; q < 4; ++q) { const int m = 2 * (mh) + (q >> 1), sx = q & 1; vn[0] = MFMA32(F[q], Sb[m][sx], vn[0]); vn[1] = MFMA32(F[4 + q], Sb[m][sx], vn[1]); } } while (0)
; #define SCAN_MMK(F, mh) do { _Pragma("unroll") for (int q = 0; q < 4; ++q) { const int j2 = q >> 1, sx = q & 1; S[2 * (mh)] = MFMA32(F[q], Vb[j2][sx], S[2 * (mh)]); S[2 * (mh) + 1] = MFMA32(F[4 + q], Vb[j2][sx], S[2 * (mh) + 1]); } } while (0)
; DI void gdn_scan_seq(const Params& p, int bh16, char* ldsf) {
;     ...
;     SCAN_RDW(fa, 0);
;     __builtin_amdgcn_sched_barrier(0);
;     SCAN_RDW(fb, 1);
;     __builtin_amdgcn_sched_barrier(0);
;     SCAN_MMW(fa, 0);
;     __builtin_amdgcn_sched_barrier(0);
;     SCAN_RDK(fa, 0);
;     __builtin_amdgcn_sched_barrier(0);
;     SCAN_MMW(fb, 1);
;     __builtin_amdgcn_sched_barrier(0);
;     SCAN_RDK(fb, 1);
;     __builtin_amdgcn_sched_barrier(0);
;     bf16x8 Vb[2][2];
; #pragma unroll
;     for (int j2 = 0; j2 < 2; ++j2) { Vb[j2][0] = packS(vn[j2], 0); Vb[j2][1] = packS(vn[j2], 1); }
; #pragma unroll
;     for (int m = 0; m < 4; ++m)
; #pragma unroll
;       for (int r = 0; r < 16; ++r) S[m][r] *= gl;
;     SCAN_MMK(fa, 0);
;     SCAN_MMK(fb, 1);
;     ...
;     asm volatile("s_waitcnt lgkmcnt(0)" ::: "memory");
;     sl = sl == 2 ? 0 : sl + 1;
;   }
	ds_read_b128 v[182:185], v131 offset:8192
	ds_read_b128 v[190:193], v131 offset:9216
	ds_read_b128 v[194:197], v131 offset:10240
	ds_read_b128 v[198:201], v131 offset:11264
	ds_read_b128 v[202:205], v131 offset:12288
	ds_read_b128 v[208:211], v131 offset:13312
	ds_read_b128 v[212:215], v131 offset:14336
	ds_read_b128 v[216:219], v131 offset:15360
	v_mfma_f32_32x32x16_bf16 v[64:79], v[148:151], v[96:99], v[64:79]
	v_cvt_pk_bf16_f32 v112, v32, v33
	v_cvt_pk_bf16_f32 v113, v34, v35
	v_cvt_pk_bf16_f32 v114, v36, v37
	v_cvt_pk_bf16_f32 v115, v38, v39
	v_cvt_pk_bf16_f32 v116, v40, v41
	v_mfma_f32_32x32x16_bf16 v[64:79], v[152:155], v[100:103], v[64:79]
	v_cvt_pk_bf16_f32 v117, v42, v43
	v_cvt_pk_bf16_f32 v118, v44, v45
	v_cvt_pk_bf16_f32 v119, v46, v47
	v_cvt_pk_bf16_f32 v120, v48, v49
	v_cvt_pk_bf16_f32 v121, v50, v51
	v_mfma_f32_32x32x16_bf16 v[64:79], v[156:159], v[104:107], v[64:79]
	v_cvt_pk_bf16_f32 v122, v52, v53
	v_cvt_pk_bf16_f32 v123, v54, v55
	v_cvt_pk_bf16_f32 v124, v56, v57
	v_cvt_pk_bf16_f32 v125, v58, v59
	v_cvt_pk_bf16_f32 v126, v60, v61
	v_mfma_f32_32x32x16_bf16 v[64:79], v[160:163], v[108:111], v[64:79]
	v_cvt_pk_bf16_f32 v127, v62, v63
	v_lshlrev_b32_e32 v80, 16, v88
	v_and_b32_e32 v81, 0xffff0000, v88
	v_lshlrev_b32_e32 v82, 16, v89
	v_and_b32_e32 v83, 0xffff0000, v89
	v_mfma_f32_32x32x16_bf16 v[64:79], v[164:167], v[112:115], v[64:79]
	v_lshlrev_b32_e32 v84, 16, v90
	v_and_b32_e32 v85, 0xffff0000, v90
	v_lshlrev_b32_e32 v86, 16, v91
	v_and_b32_e32 v87, 0xffff0000, v91
	global_store_dwordx4 v128, v[96:99], s[8:9]
	v_mfma_f32_32x32x16_bf16 v[64:79], v[168:171], v[116:119], v[64:79]
	v_lshlrev_b32_e32 v88, 16, v92
	v_and_b32_e32 v89, 0xffff0000, v92
	v_lshlrev_b32_e32 v90, 16, v93
	v_and_b32_e32 v91, 0xffff0000, v93
	global_store_dwordx4 v128, v[100:103], s[8:9] offset:1024
	v_mfma_f32_32x32x16_bf16 v[64:79], v[172:175], v[120:123], v[64:79]
	v_lshlrev_b32_e32 v92, 16, v94
	v_and_b32_e32 v93, 0xffff0000, v94
	v_lshlrev_b32_e32 v94, 16, v95
	v_and_b32_e32 v95, 0xffff0000, v95
	global_store_dwordx4 v128, v[104:107], s[8:9] offset:2048
	v_mfma_f32_32x32x16_bf16 v[64:79], v[178:181], v[124:127], v[64:79]
	v_pk_mul_f32 v[0:1], v[0:1], v[142:143] op_sel_hi:[1,0]
	v_pk_mul_f32 v[2:3], v[2:3], v[142:143] op_sel_hi:[1,0]
	v_pk_mul_f32 v[4:5], v[4:5], v[142:143] op_sel_hi:[1,0]
	v_pk_mul_f32 v[6:7], v[6:7], v[142:143] op_sel_hi:[1,0]
	global_store_dwordx4 v128, v[108:111], s[8:9] offset:3072
	s_waitcnt lgkmcnt(0)
	ds_read_b128 v[148:151], v131 offset:16384
	ds_read_b128 v[152:155], v131 offset:17408
	ds_read_b128 v[156:159], v131 offset:20480
	ds_read_b128 v[160:163], v131 offset:21504
	ds_read_b128 v[164:167], v131 offset:24576
	ds_read_b128 v[168:171], v131 offset:25600
	ds_read_b128 v[172:175], v131 offset:28672
	ds_read_b128 v[178:181], v131 offset:29696
	v_mfma_f32_32x32x16_bf16 v[80:95], v[182:185], v[96:99], v[80:95]
	v_pk_mul_f32 v[8:9], v[8:9], v[142:143] op_sel_hi:[1,0]
	v_pk_mul_f32 v[10:11], v[10:11], v[142:143] op_sel_hi:[1,0]
	v_pk_mul_f32 v[12:13], v[12:13], v[142:143] op_sel_hi:[1,0]
	v_pk_mul_f32 v[14:15], v[14:15], v[142:143] op_sel_hi:[1,0]
	global_store_dwordx4 v128, v[112:115], s[10:11]
	v_mfma_f32_32x32x16_bf16 v[80:95], v[190:193], v[100:103], v[80:95]
	v_pk_mul_f32 v[16:17], v[16:17], v[142:143] op_sel_hi:[1,0]
	v_pk_mul_f32 v[18:19], v[18:19], v[142:143] op_sel_hi:[1,0]
	v_pk_mul_f32 v[20:21], v[20:21], v[142:143] op_sel_hi:[1,0]
	v_pk_mul_f32 v[22:23], v[22:23], v[142:143] op_sel_hi:[1,0]
	global_store_dwordx4 v128, v[116:119], s[10:11] offset:1024
	v_mfma_f32_32x32x16_bf16 v[80:95], v[194:197], v[104:107], v[80:95]
	v_pk_mul_f32 v[24:25], v[24:25], v[142:143] op_sel_hi:[1,0]
	v_pk_mul_f32 v[26:27], v[26:27], v[142:143] op_sel_hi:[1,0]
	v_pk_mul_f32 v[28:29], v[28:29], v[142:143] op_sel_hi:[1,0]
	v_pk_mul_f32 v[30:31], v[30:31], v[142:143] op_sel_hi:[1,0]
	global_store_dwordx4 v128, v[120:123], s[10:11] offset:2048
	v_mfma_f32_32x32x16_bf16 v[80:95], v[198:201], v[108:111], v[80:95]
	v_pk_mul_f32 v[32:33], v[32:33], v[142:143] op_sel_hi:[1,0]
	v_pk_mul_f32 v[34:35], v[34:35], v[142:143] op_sel_hi:[1,0]
	v_pk_mul_f32 v[36:37], v[36:37], v[142:143] op_sel_hi:[1,0]
	v_pk_mul_f32 v[38:39], v[38:39], v[142:143] op_sel_hi:[1,0]
	global_store_dwordx4 v128, v[124:127], s[10:11] offset:3072
	v_mfma_f32_32x32x16_bf16 v[80:95], v[202:205], v[112:115], v[80:95]
	v_pk_mul_f32 v[40:41], v[40:41], v[142:143] op_sel_hi:[1,0]
	v_pk_mul_f32 v[42:43], v[42:43], v[142:143] op_sel_hi:[1,0]
	v_pk_mul_f32 v[44:45], v[44:45], v[142:143] op_sel_hi:[1,0]
	v_pk_mul_f32 v[46:47], v[46:47], v[142:143] op_sel_hi:[1,0]
	v_mfma_f32_32x32x16_bf16 v[80:95], v[208:211], v[116:119], v[80:95]
	v_pk_mul_f32 v[48:49], v[48:49], v[142:143] op_sel_hi:[1,0]
	v_pk_mul_f32 v[50:51], v[50:51], v[142:143] op_sel_hi:[1,0]
	v_pk_mul_f32 v[52:53], v[52:53], v[142:143] op_sel_hi:[1,0]
	v_pk_mul_f32 v[54:55], v[54:55], v[142:143] op_sel_hi:[1,0]
	v_cvt_pk_bf16_f32 v64, v64, v65
	v_mfma_f32_32x32x16_bf16 v[80:95], v[212:215], v[120:123], v[80:95]
	v_pk_mul_f32 v[56:57], v[56:57], v[142:143] op_sel_hi:[1,0]
	v_pk_mul_f32 v[58:59], v[58:59], v[142:143] op_sel_hi:[1,0]
	v_pk_mul_f32 v[60:61], v[60:61], v[142:143] op_sel_hi:[1,0]
	v_pk_mul_f32 v[62:63], v[62:63], v[142:143] op_sel_hi:[1,0]
	v_cvt_pk_bf16_f32 v65, v66, v67
	v_mfma_f32_32x32x16_bf16 v[80:95], v[216:219], v[124:127], v[80:95]
	v_cvt_pk_bf16_f32 v66, v68, v69
	v_cvt_pk_bf16_f32 v67, v70, v71
	v_cvt_pk_bf16_f32 v68, v72, v73
	v_cvt_pk_bf16_f32 v69, v74, v75
	v_cvt_pk_bf16_f32 v70, v76, v77
	v_cvt_pk_bf16_f32 v71, v78, v79
	s_waitcnt lgkmcnt(0)
	ds_read_b128 v[182:185], v131 offset:18432
	ds_read_b128 v[190:193], v131 offset:19456
	ds_read_b128 v[194:197], v131 offset:22528
	ds_read_b128 v[198:201], v131 offset:23552
	ds_read_b128 v[202:205], v131 offset:26624
	ds_read_b128 v[208:211], v131 offset:27648
	ds_read_b128 v[212:215], v131 offset:30720
	ds_read_b128 v[216:219], v131 offset:31744
	v_mfma_f32_32x32x16_bf16 v[0:15], v[148:151], v[64:67], v[0:15]
	s_add_u32 s2, s2, 1
	s_xor_b32 s3, s3, 0xc000
	s_add_u32 s18, s18, 4
	v_mfma_f32_32x32x16_bf16 v[0:15], v[152:155], v[68:71], v[0:15]
	s_add_u32 s8, s8, 0x8000
	s_addc_u32 s9, s9, 0
	s_add_u32 s10, s10, 0x8000
	s_addc_u32 s11, s11, 0
	v_mfma_f32_32x32x16_bf16 v[16:31], v[156:159], v[64:67], v[16:31]
	s_nop 0
	s_nop 0
	v_mfma_f32_32x32x16_bf16 v[16:31], v[160:163], v[68:71], v[16:31]
	v_cvt_pk_bf16_f32 v80, v80, v81
	v_cvt_pk_bf16_f32 v81, v82, v83
	v_mfma_f32_32x32x16_bf16 v[32:47], v[164:167], v[64:67], v[32:47]
	v_cvt_pk_bf16_f32 v82, v84, v85
	v_cvt_pk_bf16_f32 v83, v86, v87
	v_mfma_f32_32x32x16_bf16 v[32:47], v[168:171], v[68:71], v[32:47]
	v_cvt_pk_bf16_f32 v84, v88, v89
	v_cvt_pk_bf16_f32 v85, v90, v91
	v_mfma_f32_32x32x16_bf16 v[48:63], v[172:175], v[64:67], v[48:63]
	v_cvt_pk_bf16_f32 v86, v92, v93
	v_cvt_pk_bf16_f32 v87, v94, v95
	v_mfma_f32_32x32x16_bf16 v[48:63], v[178:181], v[68:71], v[48:63]
	s_cmp_lt_u32 s2, 0x80
	s_waitcnt lgkmcnt(0)
	s_cbranch_scc1 .Lscan_loop
	s_waitcnt vmcnt(0)
	s_barrier
; #define LAS __attribute__((address_space(3)))
; DI int tidx() { int t = threadIdx.x & 255; asm volatile("" : "+v"(t)); return t; }
; DI void phase_mixer(const Params& p, int bid, int nb, char* lds, char* ctl, char* ldsf) {
;   const int vb = threadIdx.x >> 8, lane = tidx() & 63;
;   if (bid < 32) { if (vb == 0) gdn_scan_seq(p, bid >> 1, ldsf); else { __syncthreads(); for (int k = 0; k < 128; ++k) { __builtin_amdgcn_s_barrier(); asm volatile("" ::: "memory"); } __syncthreads(); } }
;   unsigned* ctr = (unsigned*)(p.ws + WS_CTL);
;   volatile LAS int* slot = (volatile LAS int*)(ctl + 16 + 4 * vb);
.LBB0_1226:
.LBB0_1227:
	s_or_b64 exec, exec, s[0:1]
	v_readlane_b32 s2, v250, 0
	v_readfirstlane_b32 s3, v207
	s_nop 3
	s_sub_u32 s14, s2, 16
	s_cmp_lt_u32 s14, 32
	s_cbranch_scc0 .Lpf_done
	s_and_b32 s15, s3, 0xff
	s_cmp_eq_u32 s15, 0
	s_cbranch_scc0 .Lpf_done
	s_lshr_b32 s24, s14, 3
	s_and_b32 s14, s14, 7
	s_lshr_b32 s15, s3, 8
	s_lshl_b32 s15, s15, 3
	s_add_u32 s14, s14, s15
	s_lshl_b32 s15, s14, 21
	s_lshl_b32 s3, s24, 14
	s_add_u32 s15, s15, s3
	s_add_u32 s16, s84, s15
	s_addc_u32 s17, s85, 0
	s_add_u32 s18, s16, 0x1c000000
	s_addc_u32 s19, s17, 0
	s_add_u32 s16, s16, 0x1e000000
	s_addc_u32 s17, s17, 0
	s_add_u32 s22, s66, s15
	s_addc_u32 s23, s67, 0
	s_add_u32 s22, s22, 0x2000000
	s_addc_u32 s23, s23, 0
	s_lshl_b32 s15, s14, 6
	s_add_u32 s2, s84, s15
	s_addc_u32 s3, s85, 0
	s_add_u32 s2, s2, 0xc00
	s_addc_u32 s3, s3, 0
	v_mbcnt_lo_u32_b32 v0, -1, 0
	v_mbcnt_hi_u32_b32 v0, -1, v0
	v_lshlrev_b32_e32 v0, 7, v0
	v_add_u32_e32 v111, 0x2000, v0
	v_mov_b32_e32 v1, 0
	s_mov_b32 s14, s24
	s_mov_b32 s24, 0
.Lpf_loop:
	s_cmp_lt_u32 s14, 10
	s_cbranch_scc1 .Lpf_go
.Lpf_poll:
	global_load_dword v2, v1, s[2:3] sc1
	s_waitcnt vmcnt(0)
	v_readfirstlane_b32 s15, v2
	s_add_u32 s24, s24, 1
	s_add_u32 s15, s15, 10
	s_cmp_ge_u32 s15, s14
	s_cbranch_scc1 .Lpf_go
	s_cmp_gt_u32 s24, 0x1000
	s_cbranch_scc1 .Lpf_end
	s_sleep 8
	s_branch .Lpf_poll
.Lpf_go:
	global_load_dword v2, v0, s[16:17]
	global_load_dword v2, v111, s[16:17]
	global_load_dword v2, v0, s[22:23]
	global_load_dword v2, v111, s[22:23]
	global_load_dword v2, v0, s[18:19]
	global_load_dword v2, v111, s[18:19]
	s_add_u32 s16, s16, 0x10000
	s_addc_u32 s17, s17, 0
	s_add_u32 s22, s22, 0x10000
	s_addc_u32 s23, s23, 0
	s_add_u32 s18, s18, 0x10000
	s_addc_u32 s19, s19, 0
	s_add_u32 s14, s14, 4
	s_cmp_lt_u32 s14, 0x80
	s_cbranch_scc1 .Lpf_loop

; #define LAS __attribute__((address_space(3)))
; DI int tidx() { int t = threadIdx.x & 255; asm volatile("" : "+v"(t)); return t; }
; DI void phase_mixer(const Params& p, int bid, int nb, char* lds, char* ctl, char* ldsf) {
;     ...
;   unsigned* ctr = (unsigned*)(p.ws + WS_CTL);
;   volatile LAS int* slot = (volatile LAS int*)(ctl + 16 + 4 * vb);
;   volatile LAS unsigned* hbc = (volatile LAS unsigned*)(ctl + 32 + 4 * vb);
;   unsigned hbph = 0u;
;   for (;;) {
;     half_bar(hbc, hbph, lane);
;     if (tidx() == 0) *slot = (int)atomicAdd(ctr, 1u);
;     half_bar(hbc, hbph, lane);
;     const int u = *slot;
;     if (u >= 2048) break;
;     attn_unit(p, u & 31, 63 - (u >> 5), lds, hbc, hbph);
.Lpf_done:
	s_nop 4
	v_lshrrev_b32_e32 v1, 6, v207
	v_and_b32_e32 v0, 63, v135
	v_and_b32_e32 v2, 12, v1
	v_cmp_eq_u32_e64 s[0:1], 0, v0
	s_add_u32 s14, s84, 0x1900000
	v_add_u32_e32 v0, 0, v2
	v_mov_b32_e32 v1, 0
	s_addc_u32 s15, s85, 0
	s_mov_b64 s[16:17], 0
	v_add_u32_e32 v111, 0x24020, v0
	v_mov_b32_e32 v116, 1
	v_add_u32_e32 v117, 0x24010, v0
	s_movk_i32 s2, 0x800
	s_movk_i32 s3, 0x2c00
	s_mov_b32 s24, 0x3e38aa3b
	s_mov_b32 s18, 0xf800000
	v_mov_b32_e32 v118, 0x260
	s_mov_b32 s19, 0xc2fc0000
	s_mov_b32 s22, 0x800000
	s_mov_b32 s23, 0xc1f00000
	v_mov_b32_e32 v119, 0xff800000
	v_mbcnt_hi_u32_b32 v158, -1, v177
	v_mov_b32_e32 v120, 0x42800000
	v_not_b32_e32 v121, 63
	v_mov_b32_e32 v122, 0x42000000
	v_mov_b32_e32 v123, 0
	s_branch .LBB0_1230
